# baseline (speedup 1.0000x reference)
.Llg_join:
	v_add_f32_e32 v16, v16, v24
	v_add_f32_e32 v32, v32, v40
	v_add_f32_e32 v17, v17, v25
	v_add_f32_e32 v33, v33, v41
	v_add_f32_e32 v18, v18, v26
	v_add_f32_e32 v34, v34, v42
	v_add_f32_e32 v19, v19, v27
	v_add_f32_e32 v35, v35, v43
	v_add_f32_e32 v20, v20, v28
	v_add_f32_e32 v36, v36, v44
	v_add_f32_e32 v21, v21, v29
	v_add_f32_e32 v37, v37, v45
	v_add_f32_e32 v22, v22, v30
	v_add_f32_e32 v38, v38, v46
	v_add_f32_e32 v23, v23, v31
	v_add_f32_e32 v39, v39, v47
	v_add_f32_e32 v16, v16, v32
	v_add_f32_e32 v17, v17, v33
	v_add_f32_e32 v18, v18, v34
	v_add_f32_e32 v19, v19, v35
	v_add_f32_e32 v20, v20, v36
	v_add_f32_e32 v21, v21, v37
	v_add_f32_e32 v22, v22, v38
	v_add_f32_e32 v23, v23, v39
	v_mul_f32_e32 v16, v16, v48
	v_mul_f32_e32 v17, v17, v49
	v_mul_f32_e32 v18, v18, v50
	v_mul_f32_e32 v19, v19, v51
	v_mul_f32_e32 v20, v20, v52
	v_mul_f32_e32 v21, v21, v53
	v_mul_f32_e32 v22, v22, v54
	v_mul_f32_e32 v23, v23, v55
	v_max3_f32 v56, v16, v17, v18
	v_max3_f32 v57, v19, v20, v21
	v_max3_f32 v56, v56, v22, v23
	v_max_f32_e32 v56, v56, v57
	v_mov_b32_e32 v58, 0xff800000
	v_cmp_eq_u32_e32 vcc, 0, v10
	s_nop 1
	v_cndmask_b32_e32 v58, v58, v16, vcc
	v_cmp_eq_u32_e32 vcc, 1, v10
	s_nop 1
	v_cndmask_b32_e32 v58, v58, v17, vcc
	v_cmp_eq_u32_e32 vcc, 2, v10
	s_nop 1
	v_cndmask_b32_e32 v58, v58, v18, vcc
	v_cmp_eq_u32_e32 vcc, 3, v10
	s_nop 1
	v_cndmask_b32_e32 v58, v58, v19, vcc
	v_cmp_eq_u32_e32 vcc, 4, v10
	s_nop 1
	v_cndmask_b32_e32 v58, v58, v20, vcc
	v_cmp_eq_u32_e32 vcc, 5, v10
	s_nop 1
	v_cndmask_b32_e32 v58, v58, v21, vcc
	v_cmp_eq_u32_e32 vcc, 6, v10
	s_nop 1
	v_cndmask_b32_e32 v58, v58, v22, vcc
	v_cmp_eq_u32_e32 vcc, 7, v10
	s_nop 1
	v_cndmask_b32_e32 v58, v58, v23, vcc
	s_nop 1
	v_max_f32_dpp v57, v56, v56 quad_perm:[1,0,3,2] row_mask:0xf bank_mask:0xf
	s_nop 1
	v_max_f32_dpp v56, v57, v57 quad_perm:[2,3,0,1] row_mask:0xf bank_mask:0xf
	s_nop 0
	v_sub_f32_e32 v24, v16, v56
	v_sub_f32_e32 v25, v17, v56
	v_sub_f32_e32 v26, v18, v56
	v_sub_f32_e32 v27, v19, v56
	v_sub_f32_e32 v28, v20, v56
	v_sub_f32_e32 v29, v21, v56
	v_sub_f32_e32 v30, v22, v56
	v_sub_f32_e32 v31, v23, v56
	v_mul_f32_e32 v24, 0x3fb8aa3b, v24
	v_mul_f32_e32 v25, 0x3fb8aa3b, v25
	v_mul_f32_e32 v26, 0x3fb8aa3b, v26
	v_mul_f32_e32 v27, 0x3fb8aa3b, v27
	v_mul_f32_e32 v28, 0x3fb8aa3b, v28
	v_mul_f32_e32 v29, 0x3fb8aa3b, v29
	v_mul_f32_e32 v30, 0x3fb8aa3b, v30
	v_mul_f32_e32 v31, 0x3fb8aa3b, v31
	v_exp_f32_e32 v24, v24
	v_exp_f32_e32 v25, v25
	v_exp_f32_e32 v26, v26
	v_exp_f32_e32 v27, v27
	v_exp_f32_e32 v28, v28
	v_exp_f32_e32 v29, v29
	v_exp_f32_e32 v30, v30
	v_exp_f32_e32 v31, v31
	s_nop 0
	v_add_f32_e32 v24, v24, v25
	v_add_f32_e32 v26, v26, v27
	v_add_f32_e32 v28, v28, v29
	v_add_f32_e32 v30, v30, v31
	v_add_f32_e32 v24, v24, v26
	v_add_f32_e32 v28, v28, v30
	v_add_f32_e32 v59, v24, v28
	s_nop 1
	v_add_f32_dpp v60, v59, v59 quad_perm:[1,0,3,2] row_mask:0xf bank_mask:0xf
	v_max_f32_dpp v61, v58, v58 quad_perm:[1,0,3,2] row_mask:0xf bank_mask:0xf
	s_nop 1
	v_add_f32_dpp v57, v60, v60 quad_perm:[2,3,0,1] row_mask:0xf bank_mask:0xf
	v_max_f32_dpp v58, v61, v61 quad_perm:[2,3,0,1] row_mask:0xf bank_mask:0xf
	v_log_f32_e32 v57, v57
	v_cmp_eq_u32_e32 vcc, 0, v7
	v_fmac_f32_e32 v57, 0x3fb8aa3b, v56
	v_mov_b32_e32 v56, v57
	s_and_saveexec_b64 s[4:5], vcc
	s_cbranch_execz .Llg_end
	s_cmpk_ge_u32 s30, 0x80
	s_cbranch_scc1 .Llg_st1
	s_lshl_b32 s8, s3, 9
	s_lshl_b32 s9, s10, 5
	s_add_i32 s8, s8, s9
	v_add_u32_e32 v2, s8, v6
	v_lshlrev_b32_e32 v2, 2, v2
	global_store_dword v2, v56, s[24:25]
	s_cmp_lg_u32 s10, s3
	s_cbranch_scc1 .Llg_end
	v_add_u32_e32 v3, s9, v6
	v_lshlrev_b32_e32 v3, 2, v3
	global_store_dword v3, v58, s[28:29]
	s_branch .Llg_end

_Z12final_kernelPKDv4_fS1_PKfS3_Pf:
	s_load_dwordx4 s[4:7], s[0:1], 0x0
	s_load_dwordx2 s[2:3], s[0:1], 0x10
	s_load_dwordx2 s[8:9], s[0:1], 0x20
	v_and_b32_e32 v1, 0x1ff, v0
	v_readfirstlane_b32 s10, v0
	v_lshlrev_b32_e32 v3, 2, v1
	v_add_u32_e32 v4, 0x1000, v3
	v_add_u32_e32 v5, 0x2000, v3
	v_add_u32_e32 v6, 0x3000, v3
	v_add_u32_e32 v7, 0x4000, v3
	v_add_u32_e32 v8, 0x5000, v3
	v_add_u32_e32 v9, 0x6000, v3
	v_add_u32_e32 v10, 0x7000, v3
	s_cmpk_ge_u32 s10, 0x200
	s_waitcnt lgkmcnt(0)
	s_cselect_b32 s4, s6, s4
	s_cselect_b32 s5, s7, s5
	global_load_dword v12, v3, s[4:5] nt
	global_load_dword v13, v3, s[4:5] offset:2048 nt
	global_load_dword v14, v4, s[4:5] nt
	global_load_dword v15, v4, s[4:5] offset:2048 nt
	global_load_dword v16, v5, s[4:5] nt
	global_load_dword v17, v5, s[4:5] offset:2048 nt
	global_load_dword v18, v6, s[4:5] nt
	global_load_dword v19, v6, s[4:5] offset:2048 nt
	global_load_dword v20, v7, s[4:5] nt
	global_load_dword v21, v7, s[4:5] offset:2048 nt
	global_load_dword v22, v8, s[4:5] nt
	global_load_dword v23, v8, s[4:5] offset:2048 nt
	global_load_dword v24, v9, s[4:5] nt
	global_load_dword v25, v9, s[4:5] offset:2048 nt
	global_load_dword v26, v10, s[4:5] nt
	global_load_dword v27, v10, s[4:5] offset:2048 nt
	global_load_dword v44, v3, s[2:3] nt
	global_load_dword v45, v3, s[2:3] offset:2048 nt
	s_waitcnt vmcnt(2)
	v_max3_f32 v46, v12, v13, v14
	v_max3_f32 v47, v15, v16, v17
	v_max3_f32 v48, v18, v19, v20
	v_max3_f32 v49, v21, v22, v23
	v_max3_f32 v46, v46, v24, v25
	v_max3_f32 v47, v47, v26, v27
	v_max3_f32 v46, v46, v48, v49
	v_max_f32_e32 v46, v46, v47
	v_sub_f32_e32 v12, v12, v46
	v_sub_f32_e32 v13, v13, v46
	v_sub_f32_e32 v14, v14, v46
	v_sub_f32_e32 v15, v15, v46
	v_sub_f32_e32 v16, v16, v46
	v_sub_f32_e32 v17, v17, v46
	v_sub_f32_e32 v18, v18, v46
	v_sub_f32_e32 v19, v19, v46
	v_sub_f32_e32 v20, v20, v46
	v_sub_f32_e32 v21, v21, v46
	v_sub_f32_e32 v22, v22, v46
	v_sub_f32_e32 v23, v23, v46
	v_sub_f32_e32 v24, v24, v46
	v_sub_f32_e32 v25, v25, v46
	v_sub_f32_e32 v26, v26, v46
	v_sub_f32_e32 v27, v27, v46
	v_exp_f32_e32 v12, v12
	v_exp_f32_e32 v13, v13
	v_exp_f32_e32 v14, v14
	v_exp_f32_e32 v15, v15
	v_exp_f32_e32 v16, v16
	v_exp_f32_e32 v17, v17
	v_exp_f32_e32 v18, v18
	v_exp_f32_e32 v19, v19
	v_exp_f32_e32 v20, v20
	v_exp_f32_e32 v21, v21
	v_exp_f32_e32 v22, v22
	v_exp_f32_e32 v23, v23
	v_exp_f32_e32 v24, v24
	v_exp_f32_e32 v25, v25
	v_exp_f32_e32 v26, v26
	v_exp_f32_e32 v27, v27
	s_nop 0
	v_add_f32_e32 v12, v12, v20
	v_add_f32_e32 v13, v13, v21
	v_add_f32_e32 v14, v14, v22
	v_add_f32_e32 v15, v15, v23
	v_add_f32_e32 v16, v16, v24
	v_add_f32_e32 v17, v17, v25
	v_add_f32_e32 v18, v18, v26
	v_add_f32_e32 v19, v19, v27
	v_add_f32_e32 v12, v12, v16
	v_add_f32_e32 v13, v13, v17
	v_add_f32_e32 v14, v14, v18
	v_add_f32_e32 v15, v15, v19
	v_add_f32_e32 v12, v12, v14
	v_add_f32_e32 v13, v13, v15
	v_add_f32_e32 v47, v12, v13
	v_log_f32_e32 v47, v47
	s_mov_b32 s11, 0x3f317217
	v_add_f32_e32 v47, v46, v47
	v_mul_f32_e32 v48, 0x3f317217, v47
	v_fma_f32 v48, v47, s11, -v48
	v_fmamk_f32 v48, v47, 0x3377d1cf, v48
	v_fmac_f32_e32 v48, 0x3f317217, v47
	v_mov_b32_e32 v46, v48
	s_waitcnt vmcnt(0)
	v_sub_f32_e32 v46, v46, v44
	v_cmp_lt_f32_e32 vcc, 0, v45
	s_nop 1
	v_cndmask_b32_e32 v46, 0, v46, vcc
	v_cmp_lt_f32_e32 vcc, 0, v46
	v_max_f32_e32 v2, 0, v46
	s_nop 0
	v_cndmask_b32_e64 v3, 0, 1.0, vcc
	s_nop 0
	s_nop 0
	v_add_f32_dpp v2, v2, v2 quad_perm:[1,0,3,2] row_mask:0xf bank_mask:0xf
	v_add_f32_dpp v3, v3, v3 quad_perm:[1,0,3,2] row_mask:0xf bank_mask:0xf
	s_nop 0
	v_add_f32_dpp v2, v2, v2 quad_perm:[2,3,0,1] row_mask:0xf bank_mask:0xf
	v_add_f32_dpp v3, v3, v3 quad_perm:[2,3,0,1] row_mask:0xf bank_mask:0xf
	s_nop 0
	v_add_f32_dpp v2, v2, v2 row_half_mirror row_mask:0xf bank_mask:0xf
	v_add_f32_dpp v3, v3, v3 row_half_mirror row_mask:0xf bank_mask:0xf
	s_nop 0
	v_add_f32_dpp v2, v2, v2 row_mirror row_mask:0xf bank_mask:0xf
	v_add_f32_dpp v3, v3, v3 row_mirror row_mask:0xf bank_mask:0xf
	s_nop 0
	v_add_f32_dpp v2, v2, v2 row_bcast:15 row_mask:0xa bank_mask:0xf
	v_add_f32_dpp v3, v3, v3 row_bcast:15 row_mask:0xa bank_mask:0xf
	s_nop 0
	v_add_f32_dpp v2, v2, v2 row_bcast:31 row_mask:0xc bank_mask:0xf
	v_add_f32_dpp v3, v3, v3 row_bcast:31 row_mask:0xc bank_mask:0xf
	s_nop 1
	v_readlane_b32 s12, v2, 63
	v_readlane_b32 s13, v3, 63
	s_lshr_b32 s10, s10, 6
	s_lshl_b32 s10, s10, 2
	v_mov_b32_e32 v4, s10
	v_mov_b32_e32 v5, s12
	v_mov_b32_e32 v6, s13
	ds_write2_b32 v4, v5, v6 offset1:16
	s_waitcnt lgkmcnt(0)
	s_barrier
	s_cmp_lg_u32 s10, 0
	s_cbranch_scc1 .Lfin_end
	v_and_b32_e32 v4, 15, v0
	v_lshlrev_b32_e32 v4, 2, v4
	ds_read2_b32 v[2:3], v4 offset1:16
	s_waitcnt lgkmcnt(0)
	s_nop 0
	s_nop 0
	v_add_f32_dpp v2, v2, v2 quad_perm:[1,0,3,2] row_mask:0xf bank_mask:0xf
	v_add_f32_dpp v3, v3, v3 quad_perm:[1,0,3,2] row_mask:0xf bank_mask:0xf
	s_nop 0
	v_add_f32_dpp v2, v2, v2 quad_perm:[2,3,0,1] row_mask:0xf bank_mask:0xf
	v_add_f32_dpp v3, v3, v3 quad_perm:[2,3,0,1] row_mask:0xf bank_mask:0xf
	s_nop 0
	v_add_f32_dpp v2, v2, v2 row_half_mirror row_mask:0xf bank_mask:0xf
	v_add_f32_dpp v3, v3, v3 row_half_mirror row_mask:0xf bank_mask:0xf
	v_max_f32_e32 v5, 1.0, v3
	v_div_scale_f32 v6, s[12:13], v5, v5, v2
	v_rcp_f32_e32 v7, v6
	v_div_scale_f32 v8, vcc, v2, v5, v2
	v_fma_f32 v9, -v6, v7, 1.0
	v_fmac_f32_e32 v7, v9, v7
	v_mul_f32_e32 v9, v8, v7
	v_fma_f32 v10, -v6, v9, v8
	v_fmac_f32_e32 v9, v10, v7
	v_fma_f32 v6, -v6, v9, v8
	v_div_fmas_f32 v6, v6, v7, v9
	v_div_fixup_f32 v6, v6, v5, v2
	v_cmp_lt_f32_e32 vcc, 0, v3
	s_nop 1
	v_cndmask_b32_e32 v6, 0, v6, vcc
	s_nop 1
	v_add_f32_dpp v7, v6, v6 row_shl:8 row_mask:0xf bank_mask:0xf
	v_mov_b32_e32 v8, 0
	v_mul_f32_e32 v7, 0.5, v7
	v_cmp_eq_u32_e32 vcc, 0, v0
	s_and_saveexec_b64 s[12:13], vcc
	global_store_dword v8, v7, s[8:9]
